# speedup vs baseline: 1.0482x; 1.0012x over previous
.LBB0_13:
	s_andn2_b64 vcc, exec, s[4:5]
	s_cbranch_vccnz .LBB0_16
.LBB0_16:
	s_mov_b64 s[4:5], 0
.LBB0_17:
	s_andn2_b64 vcc, exec, s[4:5]
	s_cbranch_vccnz .LBB0_27
.LBB0_27:
	s_mov_b64 s[4:5], 0
.LBB0_28:
	s_andn2_b64 vcc, exec, s[4:5]
	s_cbranch_vccnz .LBB0_94
.LBB0_94:
	s_mov_b64 s[4:5], 0
